# nt hints also on P1 x-row loads, P5 LRU-pass2 coefficient loads, P17 D/OUT2 loads and output stores
# speedup vs baseline: 1.0085x; 1.0085x over previous
; DI unsigned pk_bf16(float lo, float hi) { f32x2 v = {lo, hi}; hbf16x2 r = __builtin_convertvector(v, hbf16x2); return __builtin_bit_cast(unsigned, r); }
; DI void norm_mod_store(const f32x4 (&v)[8], const float* gain, const float* shift, const float* scale, bf16_t* hrow, int lane, unsigned char* h8row = nullptr) {
;     float ss = 0.f;
; #pragma unroll
;     for (int i = 0; i < 8; ++i) ss += v[i][0] * v[i][0] + v[i][1] * v[i][1] + v[i][2] * v[i][2] + v[i][3] * v[i][3];
;     ss = wave_sum(ss);
;     const float r = rsqrtf(ss * (1.0f / DM) + EPS);
; #pragma unroll
;     for (int i = 0; i < 8; ++i) {
;         const int col = 4 * lane + 256 * i;
;         const f32x4 g = *(const f32x4*)(gain + col), sh = *(const f32x4*)(shift + col), sc = *(const f32x4*)(scale + col);
;         const f32x4 h = (v[i] * r * g) * (1.0f + sc) + sh;
;         if (h8row) *(unsigned*)(h8row + col) = pk_fp8x4(h[0], h[1], h[2], h[3]);
;         else { u32x2 w; w.x = pk_bf16(h[0], h[1]); w.y = pk_bf16(h[2], h[3]); *(u32x2*)(hrow + col) = w; }
;     }
; DI void phase_norm0(const Params& p, int G, int bid) {
;     const int lane = threadIdx.x & 63, wave = threadIdx.x >> 6;
;     const float* MOD = (const float*)(p.ws + WS_MOD);
;     bf16_t* H = (bf16_t*)(p.ws + WS_H);
;     for (int row = bid * 8 + wave; row < NTOK; row += G * 8) {
;         const float* xr = row < NCTX ? p.in[2] + (size_t)row * DM : p.in[0] + (size_t)(row - NCTX) * DM;
;         f32x4 v[8];
; #pragma unroll
;         for (int i = 0; i < 8; ++i) v[i] = *(const f32x4*)(xr + 4 * lane + 256 * i);
;         const float* md = MOD + (size_t)row_mod(row) * MODN;
;         norm_mod_store(v, p.in[9], md, md + DM, H + (size_t)row * DM, lane);
;     }
.LBB0_160:
	s_or_b64 exec, exec, s[14:15]
	v_lshl_add_u64 v[2:3], v[2:3], 0, v[36:37]
	global_load_dwordx4 v[30:33], v[2:3], off nt
	global_load_dwordx4 v[26:29], v[2:3], off offset:1024 nt
	global_load_dwordx4 v[22:25], v[2:3], off offset:2048 nt
	global_load_dwordx4 v[18:21], v[2:3], off offset:3072 nt
	v_add_co_u32_e32 v6, vcc, s18, v2
	v_lshrrev_b32_e32 v53, 11, v66
	s_nop 0
	v_addc_co_u32_e32 v7, vcc, 0, v3, vcc
	global_load_dwordx4 v[10:13], v[6:7], off offset:1024 nt
	global_load_dwordx4 v[14:17], v[6:7], off nt
	global_load_dwordx4 v[2:5], v[6:7], off offset:3072 nt
	s_nop 0
	global_load_dwordx4 v[6:9], v[6:7], off offset:2048 nt
	s_nop 0
	global_load_dwordx4 v[80:83], v[38:39], off
	v_mov_b64_e32 v[66:67], s[4:5]
	v_cndmask_b32_e64 v53, v53, 4, s[2:3]
	v_mad_u64_u32 v[66:67], s[2:3], v53, s19, v[66:67]
	v_lshl_add_u64 v[68:69], v[66:67], 0, s[12:13]
	v_lshl_add_u64 v[84:85], v[68:69], 0, v[36:37]
	v_lshl_add_u64 v[92:93], v[66:67], 0, v[36:37]
	global_load_dwordx4 v[84:87], v[84:85], off
	s_nop 0
	global_load_dwordx4 v[88:91], v[92:93], off
	v_lshlrev_b64 v[70:71], 12, v[70:71]
	v_lshl_add_u64 v[70:71], v[48:49], 0, v[70:71]
	v_mov_b32_e32 v61, v37
	v_mov_b32_e32 v63, v37
	v_mov_b32_e32 v65, v37
	v_lshl_add_u64 v[34:35], v[34:35], 0, s[6:7]
	v_lshl_add_u64 v[50:51], v[50:51], 0, s[8:9]
	s_waitcnt vmcnt(0)
	v_mul_f32_e32 v53, v31, v31
	v_mul_f32_e32 v55, v27, v27
	v_mul_f32_e32 v57, v23, v23
	v_fmac_f32_e32 v53, v30, v30
	v_fmac_f32_e32 v55, v26, v26
	v_mul_f32_e32 v59, v19, v19
	v_fmac_f32_e32 v57, v22, v22
	v_fmac_f32_e32 v53, v32, v32
	v_fmac_f32_e32 v55, v28, v28
	v_mov_b32_e32 v96, v11
	v_mov_b32_e32 v97, v15
	v_fmac_f32_e32 v59, v18, v18
	v_fmac_f32_e32 v57, v24, v24
	v_mov_b32_e32 v94, v10
	v_mov_b32_e32 v95, v14
	v_fmac_f32_e32 v53, v33, v33
	v_fmac_f32_e32 v55, v29, v29
	v_pk_mul_f32 v[96:97], v[96:97], v[96:97]
	v_fmac_f32_e32 v59, v20, v20
	v_mov_b32_e32 v98, v12
	v_mov_b32_e32 v99, v16
	v_mov_b32_e32 v104, v3
	v_mov_b32_e32 v105, v7
	v_fmac_f32_e32 v57, v25, v25
	v_add_f32_e32 v53, v53, v55
	v_pk_fma_f32 v[94:95], v[94:95], v[94:95], v[96:97]
	v_mov_b32_e32 v100, v13
	v_mov_b32_e32 v101, v17
	v_mov_b32_e32 v102, v2
	v_mov_b32_e32 v103, v6
	v_pk_mul_f32 v[104:105], v[104:105], v[104:105]
	v_fmac_f32_e32 v59, v21, v21
	v_pk_fma_f32 v[94:95], v[98:99], v[98:99], v[94:95]
	v_add_f32_e32 v53, v57, v53
	v_mov_b32_e32 v106, v4
	v_mov_b32_e32 v107, v8
	v_pk_fma_f32 v[96:97], v[102:103], v[102:103], v[104:105]
	v_add_f32_e32 v53, v59, v53
	v_pk_fma_f32 v[94:95], v[100:101], v[100:101], v[94:95]
	v_mov_b32_e32 v108, v5
	v_mov_b32_e32 v109, v9
	v_pk_fma_f32 v[96:97], v[106:107], v[106:107], v[96:97]
	v_add_f32_e32 v53, v95, v53
	v_pk_fma_f32 v[96:97], v[108:109], v[108:109], v[96:97]
	v_add_f32_e32 v53, v94, v53
	v_add_f32_e32 v53, v97, v53
	v_add_f32_e32 v53, v96, v53
	ds_bpermute_b32 v55, v1, v53
	v_pk_add_f32 v[86:87], v[86:87], 1.0 op_sel_hi:[1,0]
	v_pk_add_f32 v[84:85], v[84:85], 1.0 op_sel_hi:[1,0]
	v_mov_b32_e32 v59, v37
	s_waitcnt lgkmcnt(0)
	v_add_f32_e32 v53, v53, v55
	ds_bpermute_b32 v55, v73, v53
	s_waitcnt lgkmcnt(0)
	v_add_f32_e32 v53, v53, v55
	ds_bpermute_b32 v55, v74, v53
	s_waitcnt lgkmcnt(0)
	v_add_f32_e32 v53, v53, v55
	ds_bpermute_b32 v55, v75, v53
	s_waitcnt lgkmcnt(0)
	v_add_f32_e32 v53, v53, v55
	ds_bpermute_b32 v55, v76, v53
	s_waitcnt lgkmcnt(0)
	v_add_f32_e32 v55, v53, v55
	ds_bpermute_b32 v57, v77, v55
	v_mov_b32_e32 v53, v37
	s_waitcnt lgkmcnt(0)
	v_add_f32_e32 v55, v55, v57
	v_fmamk_f32 v55, v55, 0x3a000000, v78
	v_mul_f32_e32 v57, 0x4b800000, v55
	v_cmp_gt_f32_e32 vcc, s27, v55
	s_nop 1
	v_cndmask_b32_e32 v55, v55, v57, vcc
	v_rsq_f32_e32 v55, v55
	s_nop 0
	v_mul_f32_e32 v57, 0x45800000, v55
	v_cndmask_b32_e32 v72, v55, v57, vcc
	v_pk_mul_f32 v[32:33], v[32:33], v[72:73] op_sel_hi:[1,0]
	v_pk_mul_f32 v[30:31], v[30:31], v[72:73] op_sel_hi:[1,0]
	v_pk_mul_f32 v[32:33], v[82:83], v[32:33]
	v_pk_mul_f32 v[30:31], v[80:81], v[30:31]
	v_pk_fma_f32 v[32:33], v[86:87], v[32:33], v[90:91]
	v_pk_fma_f32 v[30:31], v[84:85], v[30:31], v[88:89]
	v_lshl_add_u64 v[80:81], v[68:69], 0, v[52:53]
	v_cvt_pk_bf16_f32 v30, v30, v31
	v_cvt_pk_bf16_f32 v31, v32, v33
	global_store_dwordx2 v[70:71], v[30:31], off
	global_load_dwordx4 v[30:33], v[38:39], off offset:1024
	s_nop 0
	global_load_dwordx4 v[80:83], v[80:81], off
	s_nop 0
	global_load_dwordx4 v[84:87], v[92:93], off offset:1024
	v_pk_mul_f32 v[28:29], v[28:29], v[72:73] op_sel_hi:[1,0]
	v_pk_mul_f32 v[26:27], v[26:27], v[72:73] op_sel_hi:[1,0]
	v_mov_b32_e32 v55, v37
	v_pk_mul_f32 v[24:25], v[24:25], v[72:73] op_sel_hi:[1,0]
	v_pk_mul_f32 v[22:23], v[22:23], v[72:73] op_sel_hi:[1,0]
	v_mov_b32_e32 v57, v37
	v_pk_mul_f32 v[20:21], v[20:21], v[72:73] op_sel_hi:[1,0]
	v_pk_mul_f32 v[18:19], v[18:19], v[72:73] op_sel_hi:[1,0]
	v_pk_mul_f32 v[16:17], v[16:17], v[72:73] op_sel_hi:[1,0]
	v_pk_mul_f32 v[14:15], v[14:15], v[72:73] op_sel_hi:[1,0]
	v_pk_mul_f32 v[12:13], v[12:13], v[72:73] op_sel_hi:[1,0]
	v_pk_mul_f32 v[10:11], v[10:11], v[72:73] op_sel_hi:[1,0]
	v_pk_mul_f32 v[8:9], v[8:9], v[72:73] op_sel_hi:[1,0]
	v_pk_mul_f32 v[6:7], v[6:7], v[72:73] op_sel_hi:[1,0]
	v_pk_mul_f32 v[4:5], v[4:5], v[72:73] op_sel_hi:[1,0]
	v_pk_mul_f32 v[2:3], v[2:3], v[72:73] op_sel_hi:[1,0]
	v_cmp_lt_i32_e32 vcc, s30, v34
	s_or_b64 s[10:11], vcc, s[10:11]
	s_waitcnt vmcnt(2)
; DI unsigned pk_bf16(float lo, float hi) { f32x2 v = {lo, hi}; hbf16x2 r = __builtin_convertvector(v, hbf16x2); return __builtin_bit_cast(unsigned, r); }
; DI void norm_mod_store(const f32x4 (&v)[8], const float* gain, const float* shift, const float* scale, bf16_t* hrow, int lane, unsigned char* h8row = nullptr) {
;     ...
;     for (int i = 0; i < 8; ++i) {
;         const int col = 4 * lane + 256 * i;
;         const f32x4 g = *(const f32x4*)(gain + col), sh = *(const f32x4*)(shift + col), sc = *(const f32x4*)(scale + col);
;         const f32x4 h = (v[i] * r * g) * (1.0f + sc) + sh;
;         if (h8row) *(unsigned*)(h8row + col) = pk_fp8x4(h[0], h[1], h[2], h[3]);
;         else { u32x2 w; w.x = pk_bf16(h[0], h[1]); w.y = pk_bf16(h[2], h[3]); *(u32x2*)(hrow + col) = w; }
;     }
	v_pk_mul_f32 v[26:27], v[30:31], v[26:27]
	v_pk_mul_f32 v[28:29], v[32:33], v[28:29]
	s_waitcnt vmcnt(1)
	v_pk_add_f32 v[30:31], v[82:83], 1.0 op_sel_hi:[1,0]
	v_pk_add_f32 v[32:33], v[80:81], 1.0 op_sel_hi:[1,0]
	s_waitcnt vmcnt(0)
	v_pk_fma_f32 v[28:29], v[30:31], v[28:29], v[86:87]
	v_pk_fma_f32 v[26:27], v[32:33], v[26:27], v[84:85]
	v_lshl_add_u64 v[30:31], v[68:69], 0, v[54:55]
	v_cvt_pk_bf16_f32 v26, v26, v27
	v_cvt_pk_bf16_f32 v27, v28, v29
	global_store_dwordx2 v[70:71], v[26:27], off offset:512
	global_load_dwordx4 v[26:29], v[38:39], off offset:2048
	s_nop 0
	global_load_dwordx4 v[30:33], v[30:31], off
	s_nop 0
	global_load_dwordx4 v[80:83], v[92:93], off offset:2048
	s_waitcnt vmcnt(2)
	v_pk_mul_f32 v[22:23], v[26:27], v[22:23]
	v_pk_mul_f32 v[24:25], v[28:29], v[24:25]
	s_waitcnt vmcnt(1)
	v_pk_add_f32 v[26:27], v[32:33], 1.0 op_sel_hi:[1,0]
	v_pk_add_f32 v[28:29], v[30:31], 1.0 op_sel_hi:[1,0]
	s_waitcnt vmcnt(0)
	v_pk_fma_f32 v[24:25], v[26:27], v[24:25], v[82:83]
	v_pk_fma_f32 v[22:23], v[28:29], v[22:23], v[80:81]
	v_lshl_add_u64 v[26:27], v[68:69], 0, v[56:57]
	v_cvt_pk_bf16_f32 v22, v22, v23
	v_cvt_pk_bf16_f32 v23, v24, v25
	global_store_dwordx2 v[70:71], v[22:23], off offset:1024
	global_load_dwordx4 v[22:25], v[38:39], off offset:3072
	s_nop 0
	global_load_dwordx4 v[26:29], v[26:27], off
	s_nop 0
	global_load_dwordx4 v[30:33], v[92:93], off offset:3072
	s_waitcnt vmcnt(2)
	v_pk_mul_f32 v[18:19], v[22:23], v[18:19]
	v_pk_mul_f32 v[20:21], v[24:25], v[20:21]
	s_waitcnt vmcnt(1)
	v_pk_add_f32 v[22:23], v[28:29], 1.0 op_sel_hi:[1,0]
	v_pk_add_f32 v[24:25], v[26:27], 1.0 op_sel_hi:[1,0]
	s_waitcnt vmcnt(0)
	v_pk_fma_f32 v[20:21], v[22:23], v[20:21], v[32:33]
	v_pk_fma_f32 v[18:19], v[24:25], v[18:19], v[30:31]
	v_lshl_add_u64 v[22:23], v[68:69], 0, v[58:59]
	v_cvt_pk_bf16_f32 v18, v18, v19
	v_cvt_pk_bf16_f32 v19, v20, v21
	global_store_dwordx2 v[70:71], v[18:19], off offset:1536
	global_load_dwordx4 v[18:21], v[40:41], off
	v_lshl_add_u64 v[26:27], v[66:67], 0, v[58:59]
	global_load_dwordx4 v[22:25], v[22:23], off
	s_waitcnt vmcnt(1)
	v_pk_mul_f32 v[14:15], v[14:15], v[18:19]
	global_load_dwordx4 v[26:29], v[26:27], off
	v_pk_mul_f32 v[16:17], v[16:17], v[20:21]
	s_waitcnt vmcnt(1)
	v_pk_add_f32 v[18:19], v[24:25], 1.0 op_sel_hi:[1,0]
	v_pk_add_f32 v[20:21], v[22:23], 1.0 op_sel_hi:[1,0]
	v_lshl_add_u64 v[22:23], v[66:67], 0, v[60:61]
	s_waitcnt vmcnt(0)
	v_pk_fma_f32 v[16:17], v[16:17], v[18:19], v[28:29]
	v_pk_fma_f32 v[14:15], v[14:15], v[20:21], v[26:27]
	v_lshl_add_u64 v[18:19], v[68:69], 0, v[60:61]
	v_cvt_pk_bf16_f32 v14, v14, v15
	v_cvt_pk_bf16_f32 v15, v16, v17
	global_store_dwordx2 v[70:71], v[14:15], off offset:2048
	global_load_dwordx4 v[14:17], v[42:43], off
	s_waitcnt vmcnt(0)
	v_pk_mul_f32 v[10:11], v[10:11], v[14:15]
	global_load_dwordx4 v[18:21], v[18:19], off
	v_pk_mul_f32 v[12:13], v[12:13], v[16:17]
	global_load_dwordx4 v[22:25], v[22:23], off
	s_waitcnt vmcnt(1)
	v_pk_add_f32 v[14:15], v[20:21], 1.0 op_sel_hi:[1,0]
	v_pk_add_f32 v[16:17], v[18:19], 1.0 op_sel_hi:[1,0]
	s_waitcnt vmcnt(0)
	v_pk_fma_f32 v[12:13], v[12:13], v[14:15], v[24:25]
	v_pk_fma_f32 v[10:11], v[10:11], v[16:17], v[22:23]
	v_lshl_add_u64 v[14:15], v[68:69], 0, v[62:63]
	v_cvt_pk_bf16_f32 v10, v10, v11
	v_cvt_pk_bf16_f32 v11, v12, v13
	global_store_dwordx2 v[70:71], v[10:11], off offset:2560
	global_load_dwordx4 v[10:13], v[44:45], off
	v_lshl_add_u64 v[18:19], v[66:67], 0, v[62:63]
	global_load_dwordx4 v[14:17], v[14:15], off
	s_waitcnt vmcnt(1)
	v_pk_mul_f32 v[6:7], v[6:7], v[10:11]
	global_load_dwordx4 v[18:21], v[18:19], off
	v_pk_mul_f32 v[8:9], v[8:9], v[12:13]
	s_waitcnt vmcnt(1)
	v_pk_add_f32 v[10:11], v[16:17], 1.0 op_sel_hi:[1,0]
	v_pk_add_f32 v[12:13], v[14:15], 1.0 op_sel_hi:[1,0]
	v_lshl_add_u64 v[14:15], v[66:67], 0, v[64:65]
	s_waitcnt vmcnt(0)
	v_pk_fma_f32 v[8:9], v[8:9], v[10:11], v[20:21]
	v_pk_fma_f32 v[6:7], v[6:7], v[12:13], v[18:19]
	v_lshl_add_u64 v[10:11], v[68:69], 0, v[64:65]
	v_cvt_pk_bf16_f32 v6, v6, v7
	v_cvt_pk_bf16_f32 v7, v8, v9
	global_store_dwordx2 v[70:71], v[6:7], off offset:3072
	global_load_dwordx4 v[6:9], v[46:47], off
	s_waitcnt vmcnt(0)
	v_pk_mul_f32 v[2:3], v[2:3], v[6:7]
	global_load_dwordx4 v[10:13], v[10:11], off
	v_pk_mul_f32 v[4:5], v[4:5], v[8:9]
	global_load_dwordx4 v[14:17], v[14:15], off
	s_waitcnt vmcnt(1)
	v_pk_add_f32 v[6:7], v[12:13], 1.0 op_sel_hi:[1,0]
	v_pk_add_f32 v[8:9], v[10:11], 1.0 op_sel_hi:[1,0]
	s_waitcnt vmcnt(0)
	v_pk_fma_f32 v[4:5], v[4:5], v[6:7], v[16:17]
	v_pk_fma_f32 v[2:3], v[2:3], v[8:9], v[14:15]
	s_nop 0
	v_cvt_pk_bf16_f32 v2, v2, v3
	v_cvt_pk_bf16_f32 v3, v4, v5
	global_store_dwordx2 v[70:71], v[2:3], off offset:3584
	s_andn2_b64 exec, exec, s[10:11]
	s_cbranch_execz .LBB0_165

; DI void lru_pass2(const Params& p, LAS unsigned char* lds, int G, int bid) {
;     ...
;     for (int u = ustart; u < uend; u += ustep) {
;         const int n = u & 7, bc = u >> 3, b = bc & 3, ci = bc >> 2;
;         const int t0 = ci < 4 ? 64 * ci : 64 * (ci - 4);
;         const int row0 = ci < 4 ? b * CTX + t0 : NCTX + b * SEQ + t0;
;         const int c4 = (tid & 31) * 4, tb = 4 * (tid >> 5), cg = 128 * n + c4;
;         u32x2 grw[4];
; #pragma unroll
;         for (int j = 0; j < 4; ++j) grw[j] = *(const u32x2*)(Z + (size_t)(row0 + tb + j) * L0INP + 1856 + cg);
;         if (tid < 256) {
;             const int sd = tid >> 7, sc = tid & 127;
;             const unsigned* ab = ABG + ((((size_t)(b * NCHUNK + ci) * 8 + n) * 2 + sd) * 64) * 128 + sc;
;             unsigned w[64];
; #pragma unroll
;             for (int t = 0; t < 64; ++t) w[t] = ab[t * 128];
;             float hh = CARRY[((size_t)(sd * NB + b) * NCHUNK + ci) * 1024 + 128 * n + sc];
.LBB0_565:
	s_bfe_u32 s6, s14, 0x20003
	s_ashr_i32 s12, s14, 5
	s_lshl_b32 s8, s12, 6
	s_lshl_b32 s11, s6, 11
	s_and_b32 s13, s14, 7
	s_add_i32 s9, s8, 0xffffff00
	s_lshl_b32 s10, s6, 8
	s_bitset1_b32 s11, 10
	s_cmp_lt_i32 s12, 4
	s_cselect_b32 s8, s8, s9
	s_cselect_b32 s54, s10, s11
	s_add_i32 s54, s54, s8
	s_lshl_b32 s8, s13, 7
	v_or_b32_e32 v6, s8, v2
	v_or_b32_e32 v20, s54, v1
	v_mad_i64_i32 v[14:15], s[10:11], v20, s17, v[10:11]
	v_lshlrev_b32_e32 v6, 1, v6
	v_lshl_add_u64 v[14:15], v[14:15], 0, v[6:7]
	v_or_b32_e32 v13, 1, v20
	v_add_co_u32_e32 v14, vcc, s18, v14
	v_mad_i64_i32 v[16:17], s[10:11], v13, s17, v[10:11]
	s_nop 0
	v_addc_co_u32_e32 v15, vcc, 0, v15, vcc
	v_lshl_add_u64 v[16:17], v[16:17], 0, v[6:7]
	v_or_b32_e32 v13, 2, v20
	v_add_co_u32_e32 v16, vcc, s18, v16
	v_mad_i64_i32 v[18:19], s[10:11], v13, s17, v[10:11]
	s_nop 0
	v_addc_co_u32_e32 v17, vcc, 0, v17, vcc
	v_lshl_add_u64 v[18:19], v[18:19], 0, v[6:7]
	v_add_co_u32_e32 v24, vcc, 0x2660e000, v18
	v_or_b32_e32 v13, 3, v20
	s_nop 0
	v_addc_co_u32_e32 v25, vcc, 0, v19, vcc
	v_mad_i64_i32 v[18:19], s[10:11], v13, s17, v[10:11]
	v_lshl_add_u64 v[18:19], v[18:19], 0, v[6:7]
	v_add_co_u32_e32 v34, vcc, 0x2660e000, v18
	s_nop 1
	v_addc_co_u32_e32 v35, vcc, 0, v19, vcc
	global_load_dwordx2 v[22:23], v[14:15], off offset:3712 nt
	global_load_dwordx2 v[18:19], v[16:17], off offset:3712 nt
	s_nop 0
	global_load_dwordx2 v[16:17], v[24:25], off offset:3712 nt
	global_load_dwordx2 v[14:15], v[34:35], off offset:3712 nt
	s_and_saveexec_b64 s[10:11], s[2:3]
	s_xor_b64 s[10:11], exec, s[10:11]
	s_mov_b32 s9, s7
	s_or_saveexec_b64 s[10:11], s[10:11]
	v_mov_b64_e32 v[24:25], s[8:9]
	s_xor_b64 exec, exec, s[10:11]
	s_cbranch_execz .LBB0_564
	s_mul_i32 s9, s6, 36
	s_add_i32 s58, s9, s12
	s_ashr_i32 s59, s58, 31
	s_lshl_b64 s[58:59], s[58:59], 4
	s_lshl_b32 s9, s13, 1
	s_or_b32 s9, s58, s9
	v_mov_b32_e32 v25, s59
	v_or_b32_e32 v24, s9, v4
	v_lshlrev_b64 v[24:25], 15, v[24:25]
	v_lshl_add_u64 v[24:25], v[8:9], 0, v[24:25]
	v_add_co_u32_e32 v34, vcc, s34, v24
	global_load_dword v93, v[24:25], off nt
	global_load_dword v92, v[24:25], off offset:512 nt
	global_load_dword v91, v[24:25], off offset:1024 nt
	global_load_dword v90, v[24:25], off offset:1536 nt
	global_load_dword v89, v[24:25], off offset:2048 nt
	global_load_dword v88, v[24:25], off offset:2560 nt
	global_load_dword v87, v[24:25], off offset:3072 nt
	global_load_dword v86, v[24:25], off offset:3584 nt
	v_addc_co_u32_e32 v35, vcc, 0, v25, vcc
	v_add_co_u32_e32 v36, vcc, s40, v24
	v_or_b32_e32 v6, s6, v3
	s_nop 0
	v_addc_co_u32_e32 v37, vcc, 0, v25, vcc
	v_add_co_u32_e32 v38, vcc, s35, v24
	global_load_dword v42, v[36:37], off offset:1536 nt
	global_load_dword v43, v[36:37], off offset:2048 nt
	global_load_dword v21, v[36:37], off offset:2560 nt
	global_load_dword v44, v[36:37], off offset:3072 nt
	global_load_dword v45, v[36:37], off offset:3584 nt
	v_addc_co_u32_e32 v39, vcc, 0, v25, vcc
	global_load_dword v46, v[38:39], off offset:3584 nt
	global_load_dword v49, v[34:35], off offset:1536 nt
	global_load_dword v48, v[34:35], off offset:2048 nt
	global_load_dword v47, v[34:35], off offset:2560 nt
	global_load_dword v50, v[34:35], off offset:3072 nt
	global_load_dword v51, v[34:35], off offset:3584 nt
	global_load_dword v52, v[36:37], off nt
	global_load_dword v53, v[36:37], off offset:512 nt
	global_load_dword v54, v[36:37], off offset:1024 nt
	global_load_dword v55, v[38:39], off offset:-4096 nt
	global_load_dword v56, v[38:39], off nt
	global_load_dword v57, v[38:39], off offset:512 nt
	global_load_dword v58, v[38:39], off offset:1024 nt
	global_load_dword v59, v[38:39], off offset:1536 nt
	global_load_dword v60, v[38:39], off offset:2048 nt
	global_load_dword v61, v[38:39], off offset:2560 nt
	global_load_dword v62, v[38:39], off offset:3072 nt
	v_add_co_u32_e32 v36, vcc, s19, v24
	v_mul_u32_u24_e32 v6, 36, v6
	s_nop 0
	v_addc_co_u32_e32 v37, vcc, 0, v25, vcc
	v_add_co_u32_e32 v38, vcc, s30, v24
	s_ashr_i32 s13, s12, 31
	s_nop 0
	v_addc_co_u32_e32 v39, vcc, 0, v25, vcc
	v_add_co_u32_e32 v40, vcc, s31, v24
	s_lshl_b32 s6, s8, 2
	s_nop 0
	v_addc_co_u32_e32 v41, vcc, 0, v25, vcc
	global_load_dword v66, v[38:39], off offset:1024 nt
	global_load_dword v65, v[38:39], off offset:1536 nt
	global_load_dword v64, v[38:39], off offset:2048 nt
	global_load_dword v63, v[38:39], off offset:2560 nt
	global_load_dword v67, v[38:39], off offset:3072 nt
	global_load_dword v68, v[38:39], off offset:3584 nt
	global_load_dword v69, v[34:35], off offset:512 nt
	global_load_dword v70, v[34:35], off offset:1024 nt
	global_load_dword v71, v[40:41], off nt
	global_load_dword v72, v[40:41], off offset:512 nt
	global_load_dword v73, v[40:41], off offset:1024 nt
	global_load_dword v74, v[40:41], off offset:1536 nt
	global_load_dword v75, v[40:41], off offset:2048 nt
	global_load_dword v76, v[40:41], off offset:2560 nt
	global_load_dword v77, v[40:41], off offset:3072 nt
	global_load_dword v78, v[40:41], off offset:3584 nt
	v_lshl_add_u64 v[34:35], v[6:7], 0, s[12:13]
	v_add_co_u32_e32 v24, vcc, s27, v24
	v_lshlrev_b64 v[34:35], 12, v[34:35]
	s_nop 0
	v_addc_co_u32_e32 v25, vcc, 0, v25, vcc
	v_lshl_add_u64 v[34:35], s[0:1], 0, v[34:35]
	global_load_dword v79, v[24:25], off offset:512 nt
	global_load_dword v80, v[24:25], off offset:1024 nt
	global_load_dword v81, v[24:25], off offset:1536 nt
	global_load_dword v82, v[24:25], off offset:2048 nt
	global_load_dword v84, v[24:25], off offset:2560 nt
	global_load_dword v85, v[24:25], off offset:3072 nt
	global_load_dword v94, v[24:25], off offset:3584 nt
	global_load_dword v95, v[40:41], off offset:-4096 nt
	global_load_dword v96, v[36:37], off offset:512 nt
	global_load_dword v97, v[36:37], off offset:1024 nt
	global_load_dword v98, v[36:37], off offset:1536 nt
	global_load_dword v99, v[36:37], off offset:2048 nt
	global_load_dword v100, v[36:37], off offset:2560 nt
	global_load_dword v101, v[36:37], off offset:3072 nt
	global_load_dword v102, v[36:37], off offset:3584 nt
	global_load_dword v103, v[38:39], off offset:512 nt
	v_lshl_add_u64 v[34:35], v[34:35], 0, s[6:7]
	v_mov_b32_e32 v13, v7
	v_lshl_add_u64 v[34:35], v[34:35], 0, v[12:13]
	global_load_dword v104, v[24:25], off offset:-4096 nt
	global_load_dword v105, v[24:25], off nt
	global_load_dword v83, v[34:35], off nt
	s_waitcnt vmcnt(62)
; DI float bflo(unsigned w) { return __uint_as_float(w << 16); }
; DI float bfhi(unsigned w) { return __uint_as_float(w & 0xffff0000u); }
; DI void lru_pass2(const Params& p, LAS unsigned char* lds, int G, int bid) {
;     ...
;             if (sd == 0) {
; #pragma unroll
;                 for (int t = 0; t < 64; ++t) { hh = fmaf(1.0f - bflo(w[t]), hh, bfhi(w[t])); HB[t * 128 + sc] = hh; }
;             } else {
; #pragma unroll
;                 for (int t = 63; t >= 0; --t) { hh = fmaf(1.0f - bflo(w[t]), hh, bfhi(w[t])); HB[(64 + t) * 128 + sc] = hh; }
	v_lshlrev_b32_e32 v169, 16, v93
	v_lshlrev_b32_e32 v168, 16, v92
	v_lshlrev_b32_e32 v167, 16, v91
	s_waitcnt vmcnt(61)
	v_lshlrev_b32_e32 v166, 16, v90
	s_waitcnt vmcnt(51)
	v_lshlrev_b32_e32 v114, 16, v46
	s_waitcnt vmcnt(50)
	v_lshlrev_b32_e32 v126, 16, v49
	s_waitcnt vmcnt(49)
	v_lshlrev_b32_e32 v125, 16, v48
	s_waitcnt vmcnt(48)
	v_lshlrev_b32_e32 v124, 16, v47
	s_waitcnt vmcnt(47)
	v_lshlrev_b32_e32 v123, 16, v50
	s_waitcnt vmcnt(46)
	v_lshlrev_b32_e32 v122, 16, v51
	s_waitcnt vmcnt(45)
	v_lshlrev_b32_e32 v113, 16, v52
	s_waitcnt vmcnt(44)
	v_lshlrev_b32_e32 v112, 16, v53
	s_waitcnt vmcnt(43)
	v_lshlrev_b32_e32 v111, 16, v54
	v_lshlrev_b32_e32 v110, 16, v42
	v_lshlrev_b32_e32 v109, 16, v43
	v_lshlrev_b32_e32 v108, 16, v21
	v_lshlrev_b32_e32 v107, 16, v44
	v_lshlrev_b32_e32 v106, 16, v45
	s_waitcnt vmcnt(37)
	v_lshlrev_b32_e32 v117, 16, v60
	s_waitcnt vmcnt(36)
	v_lshlrev_b32_e32 v116, 16, v61
	s_waitcnt vmcnt(35)
	v_lshlrev_b32_e32 v115, 16, v62
	v_lshlrev_b32_e32 v118, 16, v59
	v_lshlrev_b32_e32 v119, 16, v58
	v_lshlrev_b32_e32 v120, 16, v57
	v_lshlrev_b32_e32 v121, 16, v56
	v_lshlrev_b32_e32 v129, 16, v55
	s_waitcnt vmcnt(29)
	v_lshlrev_b32_e32 v138, 16, v68
	s_waitcnt vmcnt(28)
	v_lshlrev_b32_e32 v128, 16, v69
	s_waitcnt vmcnt(27)
	v_lshlrev_b32_e32 v127, 16, v70
	s_waitcnt vmcnt(26)
	v_lshlrev_b32_e32 v137, 16, v71
	s_waitcnt vmcnt(25)
	v_lshlrev_b32_e32 v136, 16, v72
	s_waitcnt vmcnt(24)
	v_lshlrev_b32_e32 v135, 16, v73
	s_waitcnt vmcnt(23)
	v_lshlrev_b32_e32 v134, 16, v74
	s_waitcnt vmcnt(22)
	v_lshlrev_b32_e32 v133, 16, v75
	s_waitcnt vmcnt(21)
	v_lshlrev_b32_e32 v132, 16, v76
	s_waitcnt vmcnt(20)
	v_lshlrev_b32_e32 v131, 16, v77
	s_waitcnt vmcnt(19)
	v_lshlrev_b32_e32 v130, 16, v78
	v_lshlrev_b32_e32 v139, 16, v67
	v_lshlrev_b32_e32 v140, 16, v63
	v_lshlrev_b32_e32 v141, 16, v64
	v_lshlrev_b32_e32 v142, 16, v65
	v_lshlrev_b32_e32 v143, 16, v66
	s_waitcnt vmcnt(11)
	v_lshlrev_b32_e32 v145, 16, v95
	v_lshlrev_b32_e32 v146, 16, v94
	s_waitcnt vmcnt(3)
	v_lshlrev_b32_e32 v144, 16, v103
	v_lshlrev_b32_e32 v147, 16, v85
	v_lshlrev_b32_e32 v148, 16, v84
	v_lshlrev_b32_e32 v149, 16, v82
	v_lshlrev_b32_e32 v150, 16, v81
	v_lshlrev_b32_e32 v151, 16, v80
	v_lshlrev_b32_e32 v152, 16, v79
	s_waitcnt vmcnt(1)
	v_lshlrev_b32_e32 v153, 16, v105
	v_lshlrev_b32_e32 v154, 16, v102
	v_lshlrev_b32_e32 v155, 16, v101
	v_lshlrev_b32_e32 v156, 16, v100
	v_lshlrev_b32_e32 v157, 16, v99
	v_lshlrev_b32_e32 v158, 16, v98
	v_lshlrev_b32_e32 v159, 16, v97
	v_lshlrev_b32_e32 v160, 16, v96
	v_lshlrev_b32_e32 v161, 16, v104
	v_lshlrev_b32_e32 v162, 16, v86
	v_lshlrev_b32_e32 v163, 16, v87
	v_lshlrev_b32_e32 v164, 16, v88
	v_lshlrev_b32_e32 v165, 16, v89
	v_and_b32_e32 v6, 0xffff0000, v45
	v_and_b32_e32 v13, 0xffff0000, v44
	v_and_b32_e32 v21, 0xffff0000, v21
	v_and_b32_e32 v24, 0xffff0000, v43
	v_and_b32_e32 v25, 0xffff0000, v42
	v_and_b32_e32 v34, 0xffff0000, v54
	v_and_b32_e32 v35, 0xffff0000, v53
	v_and_b32_e32 v36, 0xffff0000, v52
	v_and_b32_e32 v37, 0xffff0000, v46
	v_and_b32_e32 v38, 0xffff0000, v62
	v_and_b32_e32 v39, 0xffff0000, v61
	v_and_b32_e32 v40, 0xffff0000, v60
	v_and_b32_e32 v41, 0xffff0000, v59
	v_and_b32_e32 v42, 0xffff0000, v58
	v_and_b32_e32 v43, 0xffff0000, v57
	v_and_b32_e32 v44, 0xffff0000, v56
	v_and_b32_e32 v45, 0xffff0000, v51
	v_and_b32_e32 v46, 0xffff0000, v50
	v_and_b32_e32 v47, 0xffff0000, v47
	v_and_b32_e32 v48, 0xffff0000, v48
	v_and_b32_e32 v49, 0xffff0000, v49
	v_and_b32_e32 v50, 0xffff0000, v70
	v_and_b32_e32 v51, 0xffff0000, v69
	v_and_b32_e32 v52, 0xffff0000, v55
	v_and_b32_e32 v53, 0xffff0000, v78
	v_and_b32_e32 v54, 0xffff0000, v77
	v_and_b32_e32 v55, 0xffff0000, v76
	v_and_b32_e32 v56, 0xffff0000, v75
	v_and_b32_e32 v57, 0xffff0000, v74
	v_and_b32_e32 v58, 0xffff0000, v73
	v_and_b32_e32 v59, 0xffff0000, v72
	v_and_b32_e32 v60, 0xffff0000, v71
	v_and_b32_e32 v61, 0xffff0000, v68
	v_and_b32_e32 v62, 0xffff0000, v67
	v_and_b32_e32 v63, 0xffff0000, v63
	v_and_b32_e32 v64, 0xffff0000, v64
	v_and_b32_e32 v65, 0xffff0000, v65
	v_and_b32_e32 v66, 0xffff0000, v66
	v_and_b32_e32 v67, 0xffff0000, v103
	v_and_b32_e32 v68, 0xffff0000, v95
	v_and_b32_e32 v69, 0xffff0000, v94
	v_and_b32_e32 v70, 0xffff0000, v85
	v_and_b32_e32 v71, 0xffff0000, v84
	v_and_b32_e32 v72, 0xffff0000, v82
	v_and_b32_e32 v73, 0xffff0000, v81
	v_and_b32_e32 v74, 0xffff0000, v80
	v_and_b32_e32 v75, 0xffff0000, v79
	v_and_b32_e32 v76, 0xffff0000, v105
	v_and_b32_e32 v77, 0xffff0000, v102
	v_and_b32_e32 v78, 0xffff0000, v101
	v_and_b32_e32 v79, 0xffff0000, v100
	v_and_b32_e32 v80, 0xffff0000, v99
	v_and_b32_e32 v81, 0xffff0000, v98
	v_and_b32_e32 v82, 0xffff0000, v97
	v_and_b32_e32 v84, 0xffff0000, v96
	v_and_b32_e32 v85, 0xffff0000, v104
	v_and_b32_e32 v86, 0xffff0000, v86
	v_and_b32_e32 v87, 0xffff0000, v87
	v_and_b32_e32 v88, 0xffff0000, v88
	v_and_b32_e32 v89, 0xffff0000, v89
	v_and_b32_e32 v90, 0xffff0000, v90
	v_and_b32_e32 v91, 0xffff0000, v91
	v_and_b32_e32 v92, 0xffff0000, v92
	v_and_b32_e32 v93, 0xffff0000, v93
	v_sub_f32_e32 v94, 1.0, v106
	v_sub_f32_e32 v95, 1.0, v107
	v_sub_f32_e32 v96, 1.0, v108
	v_sub_f32_e32 v97, 1.0, v109
	v_sub_f32_e32 v98, 1.0, v110
	v_sub_f32_e32 v99, 1.0, v111
	v_sub_f32_e32 v100, 1.0, v112
	v_sub_f32_e32 v101, 1.0, v113
	v_sub_f32_e32 v102, 1.0, v114
	v_sub_f32_e32 v103, 1.0, v115
	v_sub_f32_e32 v104, 1.0, v116
	v_sub_f32_e32 v105, 1.0, v117
	v_sub_f32_e32 v106, 1.0, v118
	v_sub_f32_e32 v107, 1.0, v119
	v_sub_f32_e32 v108, 1.0, v120
; DI float bflo(unsigned w) { return __uint_as_float(w << 16); }
; DI float bfhi(unsigned w) { return __uint_as_float(w & 0xffff0000u); }
; DI void lru_pass2(const Params& p, LAS unsigned char* lds, int G, int bid) {
;     ...
;             if (sd == 0) {
; #pragma unroll
;                 for (int t = 0; t < 64; ++t) { hh = fmaf(1.0f - bflo(w[t]), hh, bfhi(w[t])); HB[t * 128 + sc] = hh; }
;             } else {
; #pragma unroll
;                 for (int t = 63; t >= 0; --t) { hh = fmaf(1.0f - bflo(w[t]), hh, bfhi(w[t])); HB[(64 + t) * 128 + sc] = hh; }
;             }
	v_sub_f32_e32 v109, 1.0, v121
	v_sub_f32_e32 v110, 1.0, v122
	v_sub_f32_e32 v111, 1.0, v123
	v_sub_f32_e32 v112, 1.0, v124
	v_sub_f32_e32 v113, 1.0, v125
	v_sub_f32_e32 v114, 1.0, v126
	v_sub_f32_e32 v115, 1.0, v127
	v_sub_f32_e32 v116, 1.0, v128
	v_sub_f32_e32 v117, 1.0, v129
	v_sub_f32_e32 v118, 1.0, v130
	v_sub_f32_e32 v119, 1.0, v131
	v_sub_f32_e32 v120, 1.0, v132
	v_sub_f32_e32 v121, 1.0, v133
	v_sub_f32_e32 v122, 1.0, v134
	v_sub_f32_e32 v123, 1.0, v135
	v_sub_f32_e32 v124, 1.0, v136
	v_sub_f32_e32 v125, 1.0, v137
	v_sub_f32_e32 v126, 1.0, v138
	v_sub_f32_e32 v127, 1.0, v139
	v_sub_f32_e32 v128, 1.0, v140
	v_sub_f32_e32 v129, 1.0, v141
	v_sub_f32_e32 v130, 1.0, v142
	v_sub_f32_e32 v131, 1.0, v143
	v_sub_f32_e32 v132, 1.0, v144
	v_sub_f32_e32 v133, 1.0, v145
	v_sub_f32_e32 v134, 1.0, v146
	v_sub_f32_e32 v135, 1.0, v147
	v_sub_f32_e32 v136, 1.0, v148
	v_sub_f32_e32 v137, 1.0, v149
	v_sub_f32_e32 v138, 1.0, v150
	v_sub_f32_e32 v139, 1.0, v151
	v_sub_f32_e32 v140, 1.0, v152
	v_sub_f32_e32 v141, 1.0, v153
	v_sub_f32_e32 v142, 1.0, v154
	v_sub_f32_e32 v143, 1.0, v155
	v_sub_f32_e32 v144, 1.0, v156
	v_sub_f32_e32 v145, 1.0, v157
	v_sub_f32_e32 v146, 1.0, v158
	v_sub_f32_e32 v147, 1.0, v159
	v_sub_f32_e32 v148, 1.0, v160
	v_sub_f32_e32 v149, 1.0, v161
	v_sub_f32_e32 v150, 1.0, v162
	v_sub_f32_e32 v151, 1.0, v163
	v_sub_f32_e32 v152, 1.0, v164
	v_sub_f32_e32 v153, 1.0, v165
	v_sub_f32_e32 v154, 1.0, v166
	v_sub_f32_e32 v155, 1.0, v167
	v_sub_f32_e32 v156, 1.0, v168
	v_sub_f32_e32 v157, 1.0, v169
	s_and_saveexec_b64 s[12:13], s[4:5]
	s_xor_b64 s[12:13], exec, s[12:13]
	s_cbranch_execz .LBB0_570
	s_waitcnt vmcnt(0)
	v_fmac_f32_e32 v6, v94, v83
	v_fmac_f32_e32 v13, v95, v6
	v_fmac_f32_e32 v21, v96, v13
	v_fmac_f32_e32 v24, v97, v21
	v_fmac_f32_e32 v25, v98, v24
	v_fmac_f32_e32 v34, v99, v25
	v_fmac_f32_e32 v35, v100, v34
	v_fmac_f32_e32 v36, v101, v35
	v_fmac_f32_e32 v37, v102, v36
	v_fmac_f32_e32 v38, v103, v37
	v_fmac_f32_e32 v39, v104, v38
	v_fmac_f32_e32 v40, v105, v39
	v_fmac_f32_e32 v41, v106, v40
	v_fmac_f32_e32 v42, v107, v41
	v_fmac_f32_e32 v43, v108, v42
	v_fmac_f32_e32 v44, v109, v43
	v_fmac_f32_e32 v45, v110, v44
	v_fmac_f32_e32 v46, v111, v45
	v_fmac_f32_e32 v47, v112, v46
	v_fmac_f32_e32 v48, v113, v47
	v_fmac_f32_e32 v49, v114, v48
	v_fmac_f32_e32 v50, v115, v49
	v_fmac_f32_e32 v51, v116, v50
	v_fmac_f32_e32 v52, v117, v51
	v_fmac_f32_e32 v53, v118, v52
	v_fmac_f32_e32 v54, v119, v53
	v_fmac_f32_e32 v55, v120, v54
	v_fmac_f32_e32 v56, v121, v55
	v_fmac_f32_e32 v57, v122, v56
	v_fmac_f32_e32 v58, v123, v57
	v_fmac_f32_e32 v59, v124, v58
	v_fmac_f32_e32 v60, v125, v59
	v_fmac_f32_e32 v61, v126, v60
	v_fmac_f32_e32 v62, v127, v61
	v_fmac_f32_e32 v63, v128, v62
	v_fmac_f32_e32 v64, v129, v63
	v_fmac_f32_e32 v65, v130, v64
	v_fmac_f32_e32 v66, v131, v65
	v_fmac_f32_e32 v67, v132, v66
	v_fmac_f32_e32 v68, v133, v67
	v_fmac_f32_e32 v69, v134, v68
	v_fmac_f32_e32 v70, v135, v69
	v_fmac_f32_e32 v71, v136, v70
	v_fmac_f32_e32 v72, v137, v71
	v_fmac_f32_e32 v73, v138, v72
	v_fmac_f32_e32 v74, v139, v73
	v_fmac_f32_e32 v75, v140, v74
	v_fmac_f32_e32 v76, v141, v75
	v_fmac_f32_e32 v77, v142, v76
	v_fmac_f32_e32 v78, v143, v77
	v_fmac_f32_e32 v79, v144, v78
	v_fmac_f32_e32 v80, v145, v79
	v_fmac_f32_e32 v81, v146, v80
	v_fmac_f32_e32 v82, v147, v81
	v_fmac_f32_e32 v84, v148, v82
	v_fmac_f32_e32 v85, v149, v84
	v_fmac_f32_e32 v86, v150, v85
	v_fmac_f32_e32 v87, v151, v86
	v_fmac_f32_e32 v88, v152, v87
	v_fmac_f32_e32 v89, v153, v88
	v_fmac_f32_e32 v90, v154, v89
	v_fmac_f32_e32 v91, v155, v90
	v_fmac_f32_e32 v92, v156, v91
	v_fmac_f32_e32 v93, v157, v92
	ds_write2st64_b32 v26, v13, v6 offset0:252 offset1:254
	ds_write2st64_b32 v26, v24, v21 offset0:248 offset1:250
	ds_write2st64_b32 v26, v34, v25 offset0:244 offset1:246
	ds_write2st64_b32 v26, v36, v35 offset0:240 offset1:242
	ds_write2st64_b32 v26, v38, v37 offset0:236 offset1:238
	ds_write2st64_b32 v26, v40, v39 offset0:232 offset1:234
	ds_write2st64_b32 v26, v42, v41 offset0:228 offset1:230
	ds_write2st64_b32 v26, v44, v43 offset0:224 offset1:226
	ds_write2st64_b32 v26, v46, v45 offset0:220 offset1:222
	ds_write2st64_b32 v26, v48, v47 offset0:216 offset1:218
	ds_write2st64_b32 v26, v50, v49 offset0:212 offset1:214
	ds_write2st64_b32 v26, v52, v51 offset0:208 offset1:210
	ds_write2st64_b32 v26, v54, v53 offset0:204 offset1:206
	ds_write2st64_b32 v26, v56, v55 offset0:200 offset1:202
	ds_write2st64_b32 v26, v58, v57 offset0:196 offset1:198
	ds_write2st64_b32 v26, v60, v59 offset0:192 offset1:194
	ds_write2st64_b32 v26, v62, v61 offset0:188 offset1:190
	ds_write2st64_b32 v26, v64, v63 offset0:184 offset1:186
	ds_write2st64_b32 v26, v66, v65 offset0:180 offset1:182
	ds_write2st64_b32 v26, v68, v67 offset0:176 offset1:178
	ds_write2st64_b32 v26, v70, v69 offset0:172 offset1:174
	ds_write2st64_b32 v26, v72, v71 offset0:168 offset1:170
	ds_write2st64_b32 v26, v74, v73 offset0:164 offset1:166
	ds_write2st64_b32 v26, v76, v75 offset0:160 offset1:162
	ds_write2st64_b32 v26, v78, v77 offset0:156 offset1:158
	ds_write2st64_b32 v26, v80, v79 offset0:152 offset1:154
	ds_write2st64_b32 v26, v82, v81 offset0:148 offset1:150
	ds_write2st64_b32 v26, v85, v84 offset0:144 offset1:146
	ds_write2st64_b32 v26, v87, v86 offset0:140 offset1:142
	ds_write2st64_b32 v26, v89, v88 offset0:136 offset1:138
	ds_write2st64_b32 v26, v91, v90 offset0:132 offset1:134
	ds_write2st64_b32 v26, v93, v92 offset0:128 offset1:130

; DI float bflo(unsigned w) { return __uint_as_float(w << 16); }
; DI float bfhi(unsigned w) { return __uint_as_float(w & 0xffff0000u); }
; template <bool FINAL>
; DI void phase_combine(const Params& p, LAS unsigned char* lds, int G, int bid, const int layer, const float* xin_ctx, const float* xin_lat, const int row_lo, const int row_hi) {
;     ...
;     for (int row = row_lo + bid * 8 + wave; row < row_hi; row += G * 8) {
;         const TokInfo ti = TOK[row];
;         const bf16_t* o0 = OUT2 + (size_t)(MT[ti.e0] + ti.p0) * DM; const bf16_t* o1 = OUT2 + (size_t)(MT[ti.e1] + ti.p1) * DM;
;         const float* xr = row < NCTX ? xin_ctx + (size_t)row * DM : xin_lat + (size_t)(row - NCTX) * DM;
;         const bf16_t* dr = (const bf16_t*)(p.ws + WS_D) + (size_t)row * DM;
;         const int mi = row_mod(row);
;         const float* g1 = MOD + ((size_t)layer * 5 + mi) * MODN + 2 * DM;
;         const float* g2 = MOD + ((size_t)layer * 5 + mi) * MODN + 5 * DM;
;         f32x4 v[8];
; #pragma unroll
;         for (int i = 0; i < 8; ++i) {
;             const int col = 4 * lane + 256 * i;
;             const u32x2 dw = *(const u32x2*)(dr + col);
;             const f32x4 x = *(const f32x4*)(xr + col) + *(const f32x4*)(g1 + col) * (f32x4){bflo(dw.x), bfhi(dw.x), bflo(dw.y), bfhi(dw.y)}, g = *(const f32x4*)(g2 + col);
;             const u32x2 a = *(const u32x2*)(o0 + col), b = *(const u32x2*)(o1 + col);
;             const f32x4 fa = {bflo(a.x), bfhi(a.x), bflo(a.y), bfhi(a.y)}, fb = {bflo(b.x), bfhi(b.x), bflo(b.y), bfhi(b.y)};
;             v[i] = x + g * (fa * ti.w0 + fb * ti.w1);
;         }
.LBB0_1848:
	s_or_b64 exec, exec, s[0:1]
	s_waitcnt lgkmcnt(0)
	v_add_u32_e32 v0, v0, v3
	v_add_u32_e32 v44, v2, v1
	v_ashrrev_i32_e32 v1, 31, v0
	v_lshrrev_b32_e32 v2, 11, v18
	v_lshl_add_u64 v[46:47], s[50:51], 0, v[24:25]
	v_lshlrev_b64 v[0:1], 12, v[0:1]
	v_add_u32_e32 v2, 5, v2
	v_add_co_u32_e64 v46, s[0:1], s25, v46
	v_lshl_add_u64 v[52:53], v[16:17], 0, v[0:1]
	v_cndmask_b32_e64 v2, v2, 9, vcc
	v_mov_b64_e32 v[0:1], s[4:5]
	v_addc_co_u32_e64 v47, s[0:1], 0, v47, s[0:1]
	v_ashrrev_i32_e32 v45, 31, v44
	v_mad_u64_u32 v[0:1], s[0:1], v2, s24, v[0:1]
	global_load_dwordx2 v[48:49], v[46:47], off nt
	global_load_dwordx2 v[58:59], v[46:47], off offset:512 nt
	v_lshlrev_b64 v[44:45], 12, v[44:45]
	v_lshl_add_u64 v[60:61], v[0:1], 0, s[18:19]
	v_lshl_add_u64 v[50:51], v[16:17], 0, v[44:45]
	v_lshl_add_u64 v[54:55], v[60:61], 0, v[4:5]
	global_load_dwordx2 v[44:45], v[50:51], off nt
	global_load_dwordx2 v[116:117], v[50:51], off offset:512 nt
	global_load_dwordx2 v[62:63], v[52:53], off nt
	global_load_dwordx2 v[118:119], v[52:53], off offset:512 nt
	v_lshl_add_u64 v[56:57], v[0:1], 0, s[20:21]
	v_lshl_add_u64 v[108:109], v[42:43], 0, v[4:5]
	global_load_dwordx4 v[0:3], v[54:55], off
	global_load_dwordx4 v[76:79], v[108:109], off
	global_load_dwordx4 v[80:83], v[108:109], off offset:1024
	v_mov_b32_e32 v27, v5
	v_lshl_add_u64 v[54:55], v[60:61], 0, v[26:27]
	global_load_dwordx4 v[84:87], v[54:55], off
	v_lshl_add_u64 v[54:55], v[56:57], 0, v[4:5]
	global_load_dwordx4 v[88:91], v[54:55], off
	v_lshl_add_u64 v[54:55], v[56:57], 0, v[26:27]
	v_mov_b32_e32 v29, v5
	global_load_dwordx4 v[92:95], v[54:55], off
	global_load_dwordx2 v[120:121], v[46:47], off offset:1024 nt
	v_lshl_add_u64 v[54:55], v[60:61], 0, v[28:29]
	global_load_dwordx4 v[96:99], v[108:109], off offset:2048
	global_load_dwordx4 v[100:103], v[54:55], off
	global_load_dwordx2 v[122:123], v[50:51], off offset:1024 nt
	global_load_dwordx2 v[124:125], v[52:53], off offset:1024 nt
	v_mov_b32_e32 v31, v5
	v_lshl_add_u64 v[128:129], v[56:57], 0, v[28:29]
	global_load_dwordx4 v[104:107], v[108:109], off offset:3072
	global_load_dwordx2 v[126:127], v[46:47], off offset:1536 nt
	global_load_dwordx2 v[66:67], v[50:51], off offset:1536 nt
	global_load_dwordx2 v[64:65], v[52:53], off offset:1536 nt
	v_lshl_add_u64 v[130:131], v[60:61], 0, v[30:31]
	global_load_dwordx4 v[108:111], v[128:129], off
	global_load_dwordx4 v[112:115], v[130:131], off
	s_waitcnt vmcnt(23)
	v_mov_b32_e32 v54, v41
	v_mov_b32_e32 v33, v5
	v_mov_b32_e32 v35, v5
	v_mov_b32_e32 v37, v5
	v_mov_b32_e32 v39, v5
	v_lshl_add_u64 v[20:21], v[20:21], 0, s[8:9]
	v_lshl_add_u64 v[22:23], v[22:23], 0, s[10:11]
	v_lshl_add_u64 v[24:25], v[24:25], 0, s[12:13]
	s_waitcnt vmcnt(22)
	v_lshlrev_b32_e32 v128, 16, v48
	v_and_b32_e32 v129, 0xffff0000, v48
	v_lshlrev_b32_e32 v48, 16, v49
	v_and_b32_e32 v49, 0xffff0000, v49
	s_waitcnt vmcnt(21)
	v_lshlrev_b32_e32 v130, 16, v58
	v_and_b32_e32 v131, 0xffff0000, v58
	s_waitcnt vmcnt(20)
	v_lshlrev_b32_e32 v132, 16, v44
	v_and_b32_e32 v133, 0xffff0000, v44
	s_waitcnt vmcnt(18)
	v_lshlrev_b32_e32 v134, 16, v62
	v_and_b32_e32 v135, 0xffff0000, v62
	v_lshlrev_b32_e32 v62, 16, v63
	s_waitcnt vmcnt(15)
	v_pk_fma_f32 v[0:1], v[0:1], v[128:129], v[76:77]
	v_lshl_add_u64 v[76:77], v[56:57], 0, v[30:31]
	v_pk_fma_f32 v[2:3], v[2:3], v[48:49], v[78:79]
	global_load_dwordx4 v[76:79], v[76:77], off
	v_and_b32_e32 v63, 0xffff0000, v63
	v_lshlrev_b32_e32 v44, 16, v45
	v_and_b32_e32 v45, 0xffff0000, v45
	v_pk_mul_f32 v[62:63], v[54:55], v[62:63] op_sel_hi:[0,1]
	v_pk_mul_f32 v[134:135], v[54:55], v[134:135] op_sel_hi:[0,1]
	v_pk_fma_f32 v[48:49], v[40:41], v[132:133], v[134:135] op_sel_hi:[0,1,1]
	v_pk_fma_f32 v[44:45], v[40:41], v[44:45], v[62:63] op_sel_hi:[0,1,1]
	s_waitcnt vmcnt(13)
	v_pk_fma_f32 v[2:3], v[90:91], v[44:45], v[2:3]
	v_pk_fma_f32 v[44:45], v[88:89], v[48:49], v[0:1]
	v_lshlrev_b32_e32 v0, 16, v119
	v_and_b32_e32 v1, 0xffff0000, v119
	v_lshlrev_b32_e32 v58, 16, v59
	v_and_b32_e32 v59, 0xffff0000, v59
	v_lshlrev_b32_e32 v136, 16, v116
	v_and_b32_e32 v137, 0xffff0000, v116
	v_lshlrev_b32_e32 v116, 16, v117
	v_and_b32_e32 v117, 0xffff0000, v117
	v_lshlrev_b32_e32 v138, 16, v118
	v_and_b32_e32 v139, 0xffff0000, v118
	v_pk_mul_f32 v[0:1], v[54:55], v[0:1] op_sel_hi:[0,1]
	v_pk_fma_f32 v[58:59], v[86:87], v[58:59], v[82:83]
	v_pk_mul_f32 v[48:49], v[54:55], v[138:139] op_sel_hi:[0,1]
	v_pk_fma_f32 v[0:1], v[40:41], v[116:117], v[0:1] op_sel_hi:[0,1,1]
	v_pk_fma_f32 v[62:63], v[84:85], v[130:131], v[80:81]
	v_pk_fma_f32 v[48:49], v[40:41], v[136:137], v[48:49] op_sel_hi:[0,1,1]
	s_waitcnt vmcnt(12)
	v_pk_fma_f32 v[0:1], v[94:95], v[0:1], v[58:59]
	v_lshl_add_u64 v[58:59], v[42:43], 0, v[32:33]
	global_load_dwordx4 v[80:83], v[58:59], off
	v_lshl_add_u64 v[58:59], v[60:61], 0, v[32:33]
	v_pk_fma_f32 v[48:49], v[92:93], v[48:49], v[62:63]
	s_waitcnt vmcnt(12)
	v_lshlrev_b32_e32 v62, 16, v121
	v_and_b32_e32 v63, 0xffff0000, v121
	global_load_dwordx4 v[84:87], v[58:59], off
	v_lshlrev_b32_e32 v58, 16, v120
	v_and_b32_e32 v59, 0xffff0000, v120
	s_waitcnt vmcnt(11)
	v_pk_fma_f32 v[62:63], v[102:103], v[62:63], v[98:99]
	s_waitcnt vmcnt(9)
; DI float bflo(unsigned w) { return __uint_as_float(w << 16); }
; DI float bfhi(unsigned w) { return __uint_as_float(w & 0xffff0000u); }
; template <bool FINAL>
; DI void phase_combine(const Params& p, LAS unsigned char* lds, int G, int bid, const int layer, const float* xin_ctx, const float* xin_lat, const int row_lo, const int row_hi) {
;     ...
; #pragma unroll
;         for (int i = 0; i < 8; ++i) {
;             const int col = 4 * lane + 256 * i;
;             const u32x2 dw = *(const u32x2*)(dr + col);
;             const f32x4 x = *(const f32x4*)(xr + col) + *(const f32x4*)(g1 + col) * (f32x4){bflo(dw.x), bfhi(dw.x), bflo(dw.y), bfhi(dw.y)}, g = *(const f32x4*)(g2 + col);
;             const u32x2 a = *(const u32x2*)(o0 + col), b = *(const u32x2*)(o1 + col);
;             const f32x4 fa = {bflo(a.x), bfhi(a.x), bflo(a.y), bfhi(a.y)}, fb = {bflo(b.x), bfhi(b.x), bflo(b.y), bfhi(b.y)};
;             v[i] = x + g * (fa * ti.w0 + fb * ti.w1);
;         }
;         if (!FINAL) {
;             if (row >= NCTX)
; #pragma unroll
;             for (int i = 0; i < 8; ++i) *(f32x4*)(XB + (size_t)row * DM + 4 * lane + 256 * i) = v[i];
;             const float* md = MOD + ((size_t)5 + mi) * MODN;
;             norm_mod_store(v, p.in[29], md, md + DM, H + (size_t)row * DM, lane, FP8_IN1 ? (unsigned char*)(p.ws + WS_H8) + (size_t)row * DM : nullptr);
;         } else {
;             float ss = 0.f;
; #pragma unroll
;             for (int i = 0; i < 8; ++i) ss += v[i][0] * v[i][0] + v[i][1] * v[i][1] + v[i][2] * v[i][2] + v[i][3] * v[i][3];
	v_lshlrev_b32_e32 v102, 16, v124
	v_and_b32_e32 v103, 0xffff0000, v124
	v_lshlrev_b32_e32 v116, 16, v125
	v_and_b32_e32 v117, 0xffff0000, v125
	global_load_dwordx2 v[128:129], v[46:47], off offset:2048 nt
	global_load_dwordx2 v[130:131], v[50:51], off offset:2048 nt
	global_load_dwordx2 v[132:133], v[52:53], off offset:2048 nt
	v_pk_fma_f32 v[134:135], v[100:101], v[58:59], v[96:97]
	v_lshlrev_b32_e32 v58, 16, v122
	v_and_b32_e32 v59, 0xffff0000, v122
	v_lshlrev_b32_e32 v100, 16, v123
	v_and_b32_e32 v101, 0xffff0000, v123
	v_pk_mul_f32 v[116:117], v[54:55], v[116:117] op_sel_hi:[0,1]
	v_pk_mul_f32 v[102:103], v[54:55], v[102:103] op_sel_hi:[0,1]
	v_lshl_add_u64 v[92:93], v[56:57], 0, v[32:33]
	v_pk_fma_f32 v[124:125], v[40:41], v[58:59], v[102:103] op_sel_hi:[0,1,1]
	v_pk_fma_f32 v[58:59], v[40:41], v[100:101], v[116:117] op_sel_hi:[0,1,1]
	global_load_dwordx4 v[88:91], v[92:93], off
	global_load_dwordx2 v[136:137], v[46:47], off offset:2560 nt
	v_lshl_add_u64 v[92:93], v[42:43], 0, v[34:35]
	v_lshl_add_u64 v[96:97], v[60:61], 0, v[34:35]
	s_waitcnt vmcnt(9)
	v_pk_fma_f32 v[58:59], v[110:111], v[58:59], v[62:63]
	v_lshl_add_u64 v[62:63], v[56:57], 0, v[34:35]
	global_load_dwordx4 v[92:95], v[92:93], off
	v_lshlrev_b32_e32 v110, 16, v127
	global_load_dwordx4 v[96:99], v[96:97], off
	v_and_b32_e32 v111, 0xffff0000, v127
	global_load_dwordx2 v[138:139], v[50:51], off offset:2560 nt
	global_load_dwordx2 v[140:141], v[52:53], off offset:2560 nt
	global_load_dwordx4 v[100:103], v[62:63], off
	global_load_dwordx2 v[142:143], v[46:47], off offset:3072 nt
	v_lshl_add_u64 v[62:63], v[42:43], 0, v[36:37]
	global_load_dwordx4 v[116:119], v[62:63], off
	v_lshl_add_u64 v[62:63], v[60:61], 0, v[36:37]
	global_load_dwordx4 v[120:123], v[62:63], off
	v_pk_fma_f32 v[62:63], v[108:109], v[124:125], v[134:135]
	v_lshlrev_b32_e32 v108, 16, v126
	v_and_b32_e32 v109, 0xffff0000, v126
	global_load_dwordx2 v[134:135], v[50:51], off offset:3072 nt
	global_load_dwordx2 v[144:145], v[52:53], off offset:3072 nt
	s_waitcnt vmcnt(18)
	v_pk_fma_f32 v[146:147], v[112:113], v[108:109], v[104:105]
	v_lshl_add_u64 v[104:105], v[56:57], 0, v[36:37]
	v_lshl_add_u64 v[42:43], v[42:43], 0, v[38:39]
	v_pk_fma_f32 v[124:125], v[114:115], v[110:111], v[106:107]
	global_load_dwordx4 v[104:107], v[104:105], off
	s_nop 0
	global_load_dwordx2 v[148:149], v[46:47], off offset:3584 nt
	global_load_dwordx4 v[108:111], v[42:43], off
	v_lshl_add_u64 v[42:43], v[60:61], 0, v[38:39]
	global_load_dwordx4 v[112:115], v[42:43], off
	global_load_dwordx2 v[150:151], v[50:51], off offset:3584 nt
	v_lshlrev_b32_e32 v42, 16, v64
	v_and_b32_e32 v43, 0xffff0000, v64
	v_lshlrev_b32_e32 v46, 16, v65
	global_load_dwordx2 v[152:153], v[52:53], off offset:3584 nt
	v_and_b32_e32 v47, 0xffff0000, v65
	v_lshlrev_b32_e32 v126, 16, v66
	v_and_b32_e32 v127, 0xffff0000, v66
	v_lshlrev_b32_e32 v66, 16, v67
	v_and_b32_e32 v67, 0xffff0000, v67
	v_pk_mul_f32 v[46:47], v[54:55], v[46:47] op_sel_hi:[0,1]
	v_pk_mul_f32 v[42:43], v[54:55], v[42:43] op_sel_hi:[0,1]
	v_pk_fma_f32 v[50:51], v[40:41], v[126:127], v[42:43] op_sel_hi:[0,1,1]
	v_pk_fma_f32 v[42:43], v[40:41], v[66:67], v[46:47] op_sel_hi:[0,1,1]
	v_lshl_add_u64 v[46:47], v[56:57], 0, v[38:39]
	s_waitcnt vmcnt(23)
	v_pk_fma_f32 v[42:43], v[78:79], v[42:43], v[124:125]
	global_load_dwordx4 v[124:127], v[46:47], off
	v_pk_fma_f32 v[46:47], v[76:77], v[50:51], v[146:147]
	v_mul_f32_e32 v19, v45, v45
	v_mul_f32_e32 v27, v49, v49
	v_fmac_f32_e32 v19, v44, v44
	v_fmac_f32_e32 v27, v48, v48
	v_fmac_f32_e32 v19, v2, v2
	v_fmac_f32_e32 v27, v0, v0
	v_fmac_f32_e32 v19, v3, v3
	v_fmac_f32_e32 v27, v1, v1
	v_add_f32_e32 v19, v19, v27
	v_mul_f32_e32 v27, v63, v63
	v_fmac_f32_e32 v27, v62, v62
	v_fmac_f32_e32 v27, v58, v58
	v_fmac_f32_e32 v27, v59, v59
	v_add_f32_e32 v19, v19, v27
	v_mul_f32_e32 v27, v47, v47
	v_fmac_f32_e32 v27, v46, v46
	v_fmac_f32_e32 v27, v42, v42
	v_fmac_f32_e32 v27, v43, v43
	v_add_f32_e32 v19, v19, v27
	s_waitcnt vmcnt(21)
	v_lshlrev_b32_e32 v50, 16, v128
	v_and_b32_e32 v51, 0xffff0000, v128
	s_waitcnt vmcnt(19)
	v_lshlrev_b32_e32 v64, 16, v132
	v_and_b32_e32 v65, 0xffff0000, v132
	v_lshlrev_b32_e32 v66, 16, v133
	v_and_b32_e32 v67, 0xffff0000, v133
	v_lshlrev_b32_e32 v52, 16, v129
	v_and_b32_e32 v53, 0xffff0000, v129
	v_pk_fma_f32 v[56:57], v[84:85], v[50:51], v[80:81]
	v_lshlrev_b32_e32 v50, 16, v130
	v_and_b32_e32 v51, 0xffff0000, v130
	v_lshlrev_b32_e32 v60, 16, v131
	v_and_b32_e32 v61, 0xffff0000, v131
	v_pk_mul_f32 v[66:67], v[54:55], v[66:67] op_sel_hi:[0,1]
	v_pk_mul_f32 v[64:65], v[54:55], v[64:65] op_sel_hi:[0,1]
	v_pk_fma_f32 v[52:53], v[86:87], v[52:53], v[82:83]
	v_pk_fma_f32 v[64:65], v[40:41], v[50:51], v[64:65] op_sel_hi:[0,1,1]
	v_pk_fma_f32 v[50:51], v[40:41], v[60:61], v[66:67] op_sel_hi:[0,1,1]
	s_waitcnt vmcnt(18)
	v_pk_fma_f32 v[50:51], v[90:91], v[50:51], v[52:53]
	v_pk_fma_f32 v[52:53], v[88:89], v[64:65], v[56:57]
	s_waitcnt vmcnt(17)
	v_lshlrev_b32_e32 v56, 16, v136
	v_and_b32_e32 v57, 0xffff0000, v136
	v_lshlrev_b32_e32 v60, 16, v137
	s_waitcnt vmcnt(13)
	v_lshlrev_b32_e32 v76, 16, v140
	v_and_b32_e32 v77, 0xffff0000, v140
	v_lshlrev_b32_e32 v78, 16, v141
	v_and_b32_e32 v79, 0xffff0000, v141
	v_and_b32_e32 v61, 0xffff0000, v137
	v_pk_fma_f32 v[64:65], v[96:97], v[56:57], v[92:93]
	v_lshlrev_b32_e32 v56, 16, v138
	v_and_b32_e32 v57, 0xffff0000, v138
	v_lshlrev_b32_e32 v66, 16, v139
	v_and_b32_e32 v67, 0xffff0000, v139
	v_pk_mul_f32 v[78:79], v[54:55], v[78:79] op_sel_hi:[0,1]
	v_pk_mul_f32 v[76:77], v[54:55], v[76:77] op_sel_hi:[0,1]
	v_pk_fma_f32 v[60:61], v[98:99], v[60:61], v[94:95]
	v_pk_fma_f32 v[76:77], v[40:41], v[56:57], v[76:77] op_sel_hi:[0,1,1]
	v_pk_fma_f32 v[56:57], v[40:41], v[66:67], v[78:79] op_sel_hi:[0,1,1]
	s_waitcnt vmcnt(12)
; template <bool FINAL>
; DI void phase_combine(const Params& p, LAS unsigned char* lds, int G, int bid, const int layer, const float* xin_ctx, const float* xin_lat, const int row_lo, const int row_hi) {
;     ...
;             float ss = 0.f;
; #pragma unroll
;             for (int i = 0; i < 8; ++i) ss += v[i][0] * v[i][0] + v[i][1] * v[i][1] + v[i][2] * v[i][2] + v[i][3] * v[i][3];
;             ss = wave_sum(ss);
;             const float r = rsqrtf(ss * (1.0f / DM) + EPS);
; #pragma unroll
;             for (int i = 0; i < 8; ++i) { const int col = 4 * lane + 256 * i; const f32x4 g = *(const f32x4*)(p.in[6] + col); *(f32x4*)(p.out + (size_t)(row - NCTX) * DM + col) = v[i] * r * g; }
	v_pk_fma_f32 v[56:57], v[102:103], v[56:57], v[60:61]
	v_pk_fma_f32 v[60:61], v[100:101], v[76:77], v[64:65]
	s_waitcnt vmcnt(11)
	v_lshlrev_b32_e32 v64, 16, v142
	v_and_b32_e32 v65, 0xffff0000, v142
	s_waitcnt vmcnt(7)
	v_lshlrev_b32_e32 v80, 16, v144
	v_and_b32_e32 v81, 0xffff0000, v144
	v_lshlrev_b32_e32 v82, 16, v145
	v_and_b32_e32 v83, 0xffff0000, v145
	v_lshlrev_b32_e32 v66, 16, v143
	v_and_b32_e32 v67, 0xffff0000, v143
	v_pk_fma_f32 v[76:77], v[120:121], v[64:65], v[116:117]
	v_lshlrev_b32_e32 v64, 16, v134
	v_and_b32_e32 v65, 0xffff0000, v134
	v_lshlrev_b32_e32 v78, 16, v135
	v_and_b32_e32 v79, 0xffff0000, v135
	v_pk_mul_f32 v[82:83], v[54:55], v[82:83] op_sel_hi:[0,1]
	v_pk_mul_f32 v[80:81], v[54:55], v[80:81] op_sel_hi:[0,1]
	v_pk_fma_f32 v[66:67], v[122:123], v[66:67], v[118:119]
	v_pk_fma_f32 v[80:81], v[40:41], v[64:65], v[80:81] op_sel_hi:[0,1,1]
	v_pk_fma_f32 v[64:65], v[40:41], v[78:79], v[82:83] op_sel_hi:[0,1,1]
	s_waitcnt vmcnt(1)
	v_lshlrev_b32_e32 v84, 16, v152
	v_and_b32_e32 v85, 0xffff0000, v152
	v_lshlrev_b32_e32 v86, 16, v153
	v_and_b32_e32 v87, 0xffff0000, v153
	v_pk_fma_f32 v[64:65], v[106:107], v[64:65], v[66:67]
	v_pk_fma_f32 v[66:67], v[104:105], v[80:81], v[76:77]
	v_lshlrev_b32_e32 v76, 16, v148
	v_and_b32_e32 v77, 0xffff0000, v148
	v_lshlrev_b32_e32 v78, 16, v149
	v_and_b32_e32 v79, 0xffff0000, v149
	v_lshlrev_b32_e32 v80, 16, v150
	v_and_b32_e32 v81, 0xffff0000, v150
	v_lshlrev_b32_e32 v82, 16, v151
	v_and_b32_e32 v83, 0xffff0000, v151
	v_pk_mul_f32 v[86:87], v[54:55], v[86:87] op_sel_hi:[0,1]
	v_pk_mul_f32 v[54:55], v[54:55], v[84:85] op_sel_hi:[0,1]
	v_pk_fma_f32 v[78:79], v[114:115], v[78:79], v[110:111]
	v_pk_fma_f32 v[76:77], v[112:113], v[76:77], v[108:109]
	v_pk_fma_f32 v[54:55], v[40:41], v[80:81], v[54:55] op_sel_hi:[0,1,1]
	v_pk_fma_f32 v[40:41], v[40:41], v[82:83], v[86:87] op_sel_hi:[0,1,1]
	s_waitcnt vmcnt(0)
	v_pk_fma_f32 v[40:41], v[126:127], v[40:41], v[78:79]
	v_pk_fma_f32 v[54:55], v[124:125], v[54:55], v[76:77]
	global_load_dwordx4 v[76:79], v[6:7], off
	v_mov_b32_e32 v82, v53
	v_mov_b32_e32 v83, v61
	v_mov_b32_e32 v80, v52
	v_mov_b32_e32 v81, v60
	v_pk_mul_f32 v[82:83], v[82:83], v[82:83]
	s_nop 0
	v_pk_fma_f32 v[80:81], v[80:81], v[80:81], v[82:83]
	v_mov_b32_e32 v82, v50
	v_mov_b32_e32 v83, v56
	v_pk_fma_f32 v[80:81], v[82:83], v[82:83], v[80:81]
	v_mov_b32_e32 v82, v51
	v_mov_b32_e32 v83, v57
	v_pk_fma_f32 v[80:81], v[82:83], v[82:83], v[80:81]
	v_mov_b32_e32 v82, v67
	v_add_f32_e32 v19, v19, v80
	v_mov_b32_e32 v83, v55
	v_add_f32_e32 v19, v19, v81
	v_mov_b32_e32 v80, v66
	v_mov_b32_e32 v81, v54
	v_pk_mul_f32 v[82:83], v[82:83], v[82:83]
	s_nop 0
	v_pk_fma_f32 v[80:81], v[80:81], v[80:81], v[82:83]
	v_mov_b32_e32 v82, v64
	v_mov_b32_e32 v83, v40
	v_pk_fma_f32 v[80:81], v[82:83], v[82:83], v[80:81]
	v_mov_b32_e32 v82, v65
	v_mov_b32_e32 v83, v41
	v_pk_fma_f32 v[80:81], v[82:83], v[82:83], v[80:81]
	s_nop 0
	v_add_f32_e32 v19, v19, v80
	v_add_f32_e32 v19, v19, v81
	ds_bpermute_b32 v27, v68, v19
	s_waitcnt lgkmcnt(0)
	v_add_f32_e32 v19, v19, v27
	ds_bpermute_b32 v27, v69, v19
	s_waitcnt lgkmcnt(0)
	v_add_f32_e32 v19, v19, v27
	ds_bpermute_b32 v27, v70, v19
	s_waitcnt lgkmcnt(0)
	v_add_f32_e32 v19, v19, v27
	ds_bpermute_b32 v27, v71, v19
	s_waitcnt lgkmcnt(0)
	v_add_f32_e32 v19, v19, v27
	ds_bpermute_b32 v27, v72, v19
	s_waitcnt lgkmcnt(0)
	v_add_f32_e32 v19, v19, v27
	ds_bpermute_b32 v27, v73, v19
	s_waitcnt lgkmcnt(0)
	v_add_f32_e32 v19, v19, v27
	v_fmamk_f32 v19, v19, 0x3a000000, v74
	v_mul_f32_e32 v27, 0x4b800000, v19
	v_cmp_gt_f32_e32 vcc, s26, v19
	s_nop 1
	v_cndmask_b32_e32 v19, v19, v27, vcc
	v_rsq_f32_e32 v19, v19
	s_nop 0
	v_mul_f32_e32 v27, 0x45800000, v19
	v_cndmask_b32_e32 v80, v19, v27, vcc
	v_ashrrev_i32_e32 v19, 31, v18
	v_lshlrev_b64 v[82:83], 13, v[18:19]
	v_pk_mul_f32 v[44:45], v[44:45], v[80:81] op_sel_hi:[1,0]
	v_pk_mul_f32 v[2:3], v[2:3], v[80:81] op_sel_hi:[1,0]
	s_waitcnt vmcnt(0)
	v_pk_mul_f32 v[76:77], v[76:77], v[44:45]
	v_lshl_add_u64 v[44:45], s[48:49], 0, v[82:83]
	v_pk_mul_f32 v[78:79], v[78:79], v[2:3]
	v_lshl_add_u64 v[82:83], v[44:45], 0, v[4:5]
	global_store_dwordx4 v[82:83], v[76:79], off nt
	global_load_dwordx4 v[76:79], v[6:7], off offset:1024
	v_pk_mul_f32 v[2:3], v[0:1], v[80:81] op_sel_hi:[1,0]
	v_pk_mul_f32 v[0:1], v[48:49], v[80:81] op_sel_hi:[1,0]
	v_pk_mul_f32 v[48:49], v[58:59], v[80:81] op_sel_hi:[1,0]
	v_pk_mul_f32 v[58:59], v[62:63], v[80:81] op_sel_hi:[1,0]
	v_pk_mul_f32 v[42:43], v[42:43], v[80:81] op_sel_hi:[1,0]
	v_pk_mul_f32 v[46:47], v[46:47], v[80:81] op_sel_hi:[1,0]
	v_add_u32_e32 v18, s6, v18
	v_add_u32_e32 v19, 0x400, v18
	v_cmp_lt_i32_e32 vcc, s27, v19
	v_pk_mul_f32 v[40:41], v[40:41], v[80:81] op_sel_hi:[1,0]
	s_or_b64 s[14:15], vcc, s[14:15]
	s_waitcnt vmcnt(0)
	v_pk_mul_f32 v[0:1], v[76:77], v[0:1]
	v_pk_mul_f32 v[2:3], v[78:79], v[2:3]
	global_store_dwordx4 v[82:83], v[0:3], off offset:1024 nt
	global_load_dwordx4 v[0:3], v[6:7], off offset:2048
	s_waitcnt vmcnt(0)
	v_pk_mul_f32 v[0:1], v[0:1], v[58:59]
	v_pk_mul_f32 v[2:3], v[2:3], v[48:49]
	global_store_dwordx4 v[82:83], v[0:3], off offset:2048 nt
	global_load_dwordx4 v[0:3], v[6:7], off offset:3072
	v_pk_mul_f32 v[48:49], v[52:53], v[80:81] op_sel_hi:[1,0]
	s_waitcnt vmcnt(0)
	v_pk_mul_f32 v[0:1], v[0:1], v[46:47]
	v_pk_mul_f32 v[2:3], v[2:3], v[42:43]
	global_store_dwordx4 v[82:83], v[0:3], off offset:3072 nt
	global_load_dwordx4 v[0:3], v[8:9], off
	v_pk_mul_f32 v[46:47], v[50:51], v[80:81] op_sel_hi:[1,0]
	v_lshl_add_u64 v[42:43], v[44:45], 0, v[32:33]
	s_waitcnt vmcnt(0)
	v_pk_mul_f32 v[0:1], v[0:1], v[48:49]
	v_pk_mul_f32 v[2:3], v[2:3], v[46:47]
	global_store_dwordx4 v[42:43], v[0:3], off nt
	global_load_dwordx4 v[0:3], v[10:11], off
	v_pk_mul_f32 v[46:47], v[56:57], v[80:81] op_sel_hi:[1,0]
	v_pk_mul_f32 v[48:49], v[60:61], v[80:81] op_sel_hi:[1,0]
	v_lshl_add_u64 v[42:43], v[44:45], 0, v[34:35]
	s_waitcnt vmcnt(0)
	v_pk_mul_f32 v[0:1], v[0:1], v[48:49]
	v_pk_mul_f32 v[2:3], v[2:3], v[46:47]
	global_store_dwordx4 v[42:43], v[0:3], off nt
	global_load_dwordx4 v[0:3], v[12:13], off
	v_pk_mul_f32 v[46:47], v[64:65], v[80:81] op_sel_hi:[1,0]
	v_pk_mul_f32 v[48:49], v[66:67], v[80:81] op_sel_hi:[1,0]
	v_lshl_add_u64 v[42:43], v[44:45], 0, v[36:37]
	s_waitcnt vmcnt(0)
	v_pk_mul_f32 v[0:1], v[0:1], v[48:49]
	v_pk_mul_f32 v[2:3], v[2:3], v[46:47]
	global_store_dwordx4 v[42:43], v[0:3], off nt
	global_load_dwordx4 v[0:3], v[14:15], off
	v_lshl_add_u64 v[42:43], v[44:45], 0, v[38:39]
	v_pk_mul_f32 v[44:45], v[54:55], v[80:81] op_sel_hi:[1,0]
	s_waitcnt vmcnt(0)
	v_pk_mul_f32 v[2:3], v[2:3], v[40:41]
	v_pk_mul_f32 v[0:1], v[0:1], v[44:45]
	global_store_dwordx4 v[42:43], v[0:3], off nt
	s_andn2_b64 exec, exec, s[14:15]
	s_cbranch_execz .LBB0_1853
